# GEMM main loops: the two whole-buffer LDS-DMA retire waits (vmcnt(6)) moved from before the phase's MFMAs to just before its closing barrier
# speedup vs baseline: 1.0019x; 1.0019x over previous
.LBB0_371:
	s_add_i32 s31, s24, 2
	s_add_u32 s45, s56, s29
	s_addc_u32 s25, s57, s30
	s_add_i32 s64, 0, 0x10000
	v_add_u32_e32 v0, s64, v139
	s_add_u32 s66, s20, s29
	ds_read_b128 v[146:149], v0
	ds_read_b128 v[150:153], v0 offset:1024
	ds_read_b128 v[154:157], v0 offset:2048
	ds_read_b128 v[158:161], v0 offset:3072
	s_addc_u32 s67, s21, s30
	s_add_u32 s66, s66, 0xffffff80
	s_addc_u32 s67, s67, -1
	s_add_i32 s71, s64, s26
	s_add_i32 m0, s46, 0xc000
	s_add_i32 s70, s46, 0xe000
	s_add_i32 s81, 0, 0x14000
	s_add_i32 s84, s71, 0x2000
	s_cmp_eq_u32 s79, s24
	s_cselect_b32 s24, s42, s45
	s_cselect_b32 s25, s43, s25
	s_cselect_b32 s45, 0, s30
	s_cselect_b32 s64, 0, s29
	v_mov_b32_e32 v0, v134
	ds_read_b128 v[162:165], v141
	ds_read_b128 v[166:169], v141 offset:1024
	ds_read_b128 v[170:173], v141 offset:2048
	ds_read_b128 v[190:193], v141 offset:3072
	ds_read_b128 v[194:197], v141 offset:4096
	ds_read_b128 v[198:201], v141 offset:5120
	ds_read_b128 v[202:205], v141 offset:6144
	ds_read_b128 v[206:209], v141 offset:7168
	s_nop 0
	global_load_lds_dwordx4 v0, s[66:67]
	v_mov_b32_e32 v0, v136
	s_mov_b32 m0, s70
	s_nop 0
	global_load_lds_dwordx4 v0, s[66:67]
	s_waitcnt lgkmcnt(8)
	s_barrier
	s_waitcnt lgkmcnt(0)
	s_setprio 1
	s_waitcnt lgkmcnt(0)
	v_mfma_f32_16x16x32_bf16 v[120:123], v[146:149], v[162:165], v[120:123]
	v_mfma_f32_16x16x32_bf16 v[116:119], v[154:157], v[162:165], v[116:119]
	v_mfma_f32_16x16x32_bf16 v[104:107], v[146:149], v[170:173], v[104:107]
	v_mfma_f32_16x16x32_bf16 v[100:103], v[154:157], v[170:173], v[100:103]
	v_mfma_f32_16x16x32_bf16 v[92:95], v[146:149], v[194:197], v[92:95]
	v_mfma_f32_16x16x32_bf16 v[84:87], v[154:157], v[194:197], v[84:87]
	v_mfma_f32_16x16x32_bf16 v[76:79], v[146:149], v[202:205], v[76:79]
	v_mfma_f32_16x16x32_bf16 v[68:71], v[154:157], v[202:205], v[68:71]
	v_mfma_f32_16x16x32_bf16 v[120:123], v[150:153], v[166:169], v[120:123]
	v_mfma_f32_16x16x32_bf16 v[116:119], v[158:161], v[166:169], v[116:119]
	v_mfma_f32_16x16x32_bf16 v[104:107], v[150:153], v[190:193], v[104:107]
	v_mfma_f32_16x16x32_bf16 v[100:103], v[158:161], v[190:193], v[100:103]
	v_mfma_f32_16x16x32_bf16 v[92:95], v[150:153], v[198:201], v[92:95]
	v_mfma_f32_16x16x32_bf16 v[84:87], v[158:161], v[198:201], v[84:87]
	v_mfma_f32_16x16x32_bf16 v[76:79], v[150:153], v[206:209], v[76:79]
	v_mfma_f32_16x16x32_bf16 v[68:71], v[158:161], v[206:209], v[68:71]
	s_setprio 0
	s_barrier
	v_add_u32_e32 v0, s81, v139
	ds_read_b128 v[210:213], v0
	ds_read_b128 v[214:217], v0 offset:1024
	ds_read_b128 v[218:221], v0 offset:2048
	ds_read_b128 v[222:225], v0 offset:3072
	s_mov_b64 s[66:67], s[24:25]
	v_mov_b32_e32 v0, v135
	s_mov_b32 m0, s71
	s_nop 0
	global_load_lds_dwordx4 v0, s[66:67]
	v_mov_b32_e32 v0, v137
	s_mov_b32 m0, s84
	s_nop 0
	global_load_lds_dwordx4 v0, s[66:67]
	s_barrier
	s_waitcnt lgkmcnt(0)
	s_setprio 1
	s_waitcnt lgkmcnt(0)
	v_mfma_f32_16x16x32_bf16 v[128:131], v[210:213], v[162:165], v[128:131]
	v_mfma_f32_16x16x32_bf16 v[124:127], v[218:221], v[162:165], v[124:127]
	v_mfma_f32_16x16x32_bf16 v[112:115], v[210:213], v[170:173], v[112:115]
	v_mfma_f32_16x16x32_bf16 v[108:111], v[218:221], v[170:173], v[108:111]
	v_mfma_f32_16x16x32_bf16 v[96:99], v[210:213], v[194:197], v[96:99]
	v_mfma_f32_16x16x32_bf16 v[88:91], v[218:221], v[194:197], v[88:91]
	v_mfma_f32_16x16x32_bf16 v[80:83], v[210:213], v[202:205], v[80:83]
	v_mfma_f32_16x16x32_bf16 v[72:75], v[218:221], v[202:205], v[72:75]
	v_mfma_f32_16x16x32_bf16 v[128:131], v[214:217], v[166:169], v[128:131]
	v_mfma_f32_16x16x32_bf16 v[124:127], v[222:225], v[166:169], v[124:127]
	v_mfma_f32_16x16x32_bf16 v[112:115], v[214:217], v[190:193], v[112:115]
	v_mfma_f32_16x16x32_bf16 v[108:111], v[222:225], v[190:193], v[108:111]
	v_mfma_f32_16x16x32_bf16 v[96:99], v[214:217], v[198:201], v[96:99]
	v_mfma_f32_16x16x32_bf16 v[88:91], v[222:225], v[198:201], v[88:91]
	v_mfma_f32_16x16x32_bf16 v[80:83], v[214:217], v[206:209], v[80:83]
	v_mfma_f32_16x16x32_bf16 v[72:75], v[222:225], v[206:209], v[72:75]
	s_setprio 0
	s_cselect_b32 s85, s48, s58
	s_cselect_b32 s84, s49, s59
	s_add_u32 s66, s85, s64
	s_addc_u32 s67, s84, s45
	s_mov_b64 s[70:71], s[66:67]
	v_mov_b32_e32 v0, v134
	s_mov_b32 m0, s46
	s_barrier
	ds_read_b128 v[162:165], v141 offset:16384
	ds_read_b128 v[166:169], v141 offset:17408
	ds_read_b128 v[170:173], v141 offset:18432
	ds_read_b128 v[190:193], v141 offset:19456
	ds_read_b128 v[194:197], v141 offset:20480
	ds_read_b128 v[198:201], v141 offset:21504
	ds_read_b128 v[202:205], v141 offset:22528
	ds_read_b128 v[206:209], v141 offset:23552
	s_nop 0
	global_load_lds_dwordx4 v0, s[70:71]
	v_mov_b32_e32 v0, v136
	s_mov_b32 m0, s47
	s_nop 0
	global_load_lds_dwordx4 v0, s[70:71]
	s_barrier
	s_waitcnt lgkmcnt(0)
	s_setprio 1
	s_waitcnt lgkmcnt(0)
	v_mfma_f32_16x16x32_bf16 v[56:59], v[146:149], v[162:165], v[56:59]
	v_mfma_f32_16x16x32_bf16 v[52:55], v[154:157], v[162:165], v[52:55]
	v_mfma_f32_16x16x32_bf16 v[40:43], v[146:149], v[170:173], v[40:43]
	v_mfma_f32_16x16x32_bf16 v[36:39], v[154:157], v[170:173], v[36:39]
	v_mfma_f32_16x16x32_bf16 v[24:27], v[146:149], v[194:197], v[24:27]
	v_mfma_f32_16x16x32_bf16 v[20:23], v[154:157], v[194:197], v[20:23]
	v_mfma_f32_16x16x32_bf16 v[12:15], v[146:149], v[202:205], v[12:15]
	v_mfma_f32_16x16x32_bf16 v[8:11], v[154:157], v[202:205], v[8:11]
	v_mfma_f32_16x16x32_bf16 v[56:59], v[150:153], v[166:169], v[56:59]
	v_mfma_f32_16x16x32_bf16 v[52:55], v[158:161], v[166:169], v[52:55]
	v_mfma_f32_16x16x32_bf16 v[40:43], v[150:153], v[190:193], v[40:43]
	v_mfma_f32_16x16x32_bf16 v[36:39], v[158:161], v[190:193], v[36:39]
	v_mfma_f32_16x16x32_bf16 v[24:27], v[150:153], v[198:201], v[24:27]
	v_mfma_f32_16x16x32_bf16 v[20:23], v[158:161], v[198:201], v[20:23]
	v_mfma_f32_16x16x32_bf16 v[12:15], v[150:153], v[206:209], v[12:15]
	v_mfma_f32_16x16x32_bf16 v[8:11], v[158:161], v[206:209], v[8:11]
	s_setprio 0
	s_barrier
	s_add_u32 s70, s24, s6
	s_addc_u32 s71, s25, s7
	v_mov_b32_e32 v0, v135
	s_add_i32 s81, s81, s26
	s_mov_b32 m0, s81
	s_nop 0
	global_load_lds_dwordx4 v0, s[70:71]
	v_mov_b32_e32 v0, v137
	s_add_i32 m0, s81, 0x2000
	s_nop 0
	global_load_lds_dwordx4 v0, s[70:71]
	s_barrier
	s_setprio 1
	v_mfma_f32_16x16x32_bf16 v[64:67], v[210:213], v[162:165], v[64:67]
	v_mfma_f32_16x16x32_bf16 v[60:63], v[218:221], v[162:165], v[60:63]
	v_mfma_f32_16x16x32_bf16 v[48:51], v[210:213], v[170:173], v[48:51]
	v_mfma_f32_16x16x32_bf16 v[44:47], v[218:221], v[170:173], v[44:47]
	v_mfma_f32_16x16x32_bf16 v[32:35], v[210:213], v[194:197], v[32:35]
	v_mfma_f32_16x16x32_bf16 v[28:31], v[218:221], v[194:197], v[28:31]
	v_mfma_f32_16x16x32_bf16 v[16:19], v[210:213], v[202:205], v[16:19]
	v_mfma_f32_16x16x32_bf16 v[4:7], v[218:221], v[202:205], v[4:7]
	v_mfma_f32_16x16x32_bf16 v[64:67], v[214:217], v[166:169], v[64:67]
	v_mfma_f32_16x16x32_bf16 v[60:63], v[222:225], v[166:169], v[60:63]
	v_mfma_f32_16x16x32_bf16 v[48:51], v[214:217], v[190:193], v[48:51]
	v_mfma_f32_16x16x32_bf16 v[44:47], v[222:225], v[190:193], v[44:47]
	v_mfma_f32_16x16x32_bf16 v[32:35], v[214:217], v[198:201], v[32:35]
	v_mfma_f32_16x16x32_bf16 v[28:31], v[222:225], v[198:201], v[28:31]
	v_mfma_f32_16x16x32_bf16 v[16:19], v[214:217], v[206:209], v[16:19]
	v_mfma_f32_16x16x32_bf16 v[4:7], v[222:225], v[206:209], v[4:7]
	s_setprio 0
	s_add_i32 s81, 0, 0x18000
	v_add_u32_e32 v0, s81, v139
	s_waitcnt vmcnt(6)
	s_barrier
	ds_read_b128 v[146:149], v0
	ds_read_b128 v[150:153], v0 offset:1024
	ds_read_b128 v[154:157], v0 offset:2048
	ds_read_b128 v[158:161], v0 offset:3072
	s_add_u32 s70, s85, s0
	s_addc_u32 s71, s84, s1
	s_add_u32 s70, s70, s64
	s_addc_u32 s71, s71, s45
	v_mov_b32_e32 v0, v134
	s_mov_b32 m0, s51
	ds_read_b128 v[162:165], v141 offset:32768
	ds_read_b128 v[166:169], v141 offset:33792
	ds_read_b128 v[170:173], v141 offset:34816
	ds_read_b128 v[190:193], v141 offset:35840
	ds_read_b128 v[194:197], v141 offset:36864
	ds_read_b128 v[198:201], v141 offset:37888
	ds_read_b128 v[202:205], v141 offset:38912
	ds_read_b128 v[206:209], v141 offset:39936
	s_nop 0
	global_load_lds_dwordx4 v0, s[70:71]
	v_mov_b32_e32 v0, v136
	s_mov_b32 m0, s53
	s_nop 0
	global_load_lds_dwordx4 v0, s[70:71]
	s_waitcnt lgkmcnt(8)
	s_barrier
	s_waitcnt lgkmcnt(0)
	s_setprio 1
	s_waitcnt lgkmcnt(0)
	v_mfma_f32_16x16x32_bf16 v[120:123], v[146:149], v[162:165], v[120:123]
	v_mfma_f32_16x16x32_bf16 v[116:119], v[154:157], v[162:165], v[116:119]
	v_mfma_f32_16x16x32_bf16 v[104:107], v[146:149], v[170:173], v[104:107]
	v_mfma_f32_16x16x32_bf16 v[100:103], v[154:157], v[170:173], v[100:103]
	v_mfma_f32_16x16x32_bf16 v[92:95], v[146:149], v[194:197], v[92:95]
	v_mfma_f32_16x16x32_bf16 v[84:87], v[154:157], v[194:197], v[84:87]
	v_mfma_f32_16x16x32_bf16 v[76:79], v[146:149], v[202:205], v[76:79]
	v_mfma_f32_16x16x32_bf16 v[68:71], v[154:157], v[202:205], v[68:71]
	v_mfma_f32_16x16x32_bf16 v[120:123], v[150:153], v[166:169], v[120:123]
	v_mfma_f32_16x16x32_bf16 v[116:119], v[158:161], v[166:169], v[116:119]
	v_mfma_f32_16x16x32_bf16 v[104:107], v[150:153], v[190:193], v[104:107]
	v_mfma_f32_16x16x32_bf16 v[100:103], v[158:161], v[190:193], v[100:103]
	v_mfma_f32_16x16x32_bf16 v[92:95], v[150:153], v[198:201], v[92:95]
	v_mfma_f32_16x16x32_bf16 v[84:87], v[158:161], v[198:201], v[84:87]
	v_mfma_f32_16x16x32_bf16 v[76:79], v[150:153], v[206:209], v[76:79]
	v_mfma_f32_16x16x32_bf16 v[68:71], v[158:161], v[206:209], v[68:71]
	s_setprio 0
	s_barrier
	s_add_i32 s45, 0, 0x1c000
	s_add_u32 s24, s24, 0x80
	v_add_u32_e32 v0, s45, v139
	s_addc_u32 s25, s25, 0
	ds_read_b128 v[210:213], v0
	ds_read_b128 v[214:217], v0 offset:1024
	ds_read_b128 v[218:221], v0 offset:2048
	ds_read_b128 v[222:225], v0 offset:3072
	s_mov_b64 s[70:71], s[24:25]
	v_mov_b32_e32 v0, v135
	s_add_i32 s64, s81, s26
	s_mov_b32 m0, s64
	s_nop 0
	global_load_lds_dwordx4 v0, s[70:71]
	v_mov_b32_e32 v0, v137
	s_add_i32 m0, s64, 0x2000
	s_nop 0
	global_load_lds_dwordx4 v0, s[70:71]
	s_barrier
	s_waitcnt lgkmcnt(0)
	s_setprio 1
	s_waitcnt lgkmcnt(0)
	v_mfma_f32_16x16x32_bf16 v[128:131], v[210:213], v[162:165], v[128:131]
	v_mfma_f32_16x16x32_bf16 v[124:127], v[218:221], v[162:165], v[124:127]
	v_mfma_f32_16x16x32_bf16 v[112:115], v[210:213], v[170:173], v[112:115]
	v_mfma_f32_16x16x32_bf16 v[108:111], v[218:221], v[170:173], v[108:111]
	v_mfma_f32_16x16x32_bf16 v[96:99], v[210:213], v[194:197], v[96:99]
	v_mfma_f32_16x16x32_bf16 v[88:91], v[218:221], v[194:197], v[88:91]
	v_mfma_f32_16x16x32_bf16 v[80:83], v[210:213], v[202:205], v[80:83]
	v_mfma_f32_16x16x32_bf16 v[72:75], v[218:221], v[202:205], v[72:75]
	v_mfma_f32_16x16x32_bf16 v[128:131], v[214:217], v[166:169], v[128:131]
	v_mfma_f32_16x16x32_bf16 v[124:127], v[222:225], v[166:169], v[124:127]
	v_mfma_f32_16x16x32_bf16 v[112:115], v[214:217], v[190:193], v[112:115]
	v_mfma_f32_16x16x32_bf16 v[108:111], v[222:225], v[190:193], v[108:111]
	v_mfma_f32_16x16x32_bf16 v[96:99], v[214:217], v[198:201], v[96:99]
	v_mfma_f32_16x16x32_bf16 v[88:91], v[222:225], v[198:201], v[88:91]
	v_mfma_f32_16x16x32_bf16 v[80:83], v[214:217], v[206:209], v[80:83]
	v_mfma_f32_16x16x32_bf16 v[72:75], v[222:225], v[206:209], v[72:75]
	s_setprio 0
	s_add_u32 s66, s66, 0x80
	s_addc_u32 s67, s67, 0
	v_mov_b32_e32 v0, v134
	s_mov_b32 m0, s55
	s_barrier
	ds_read_b128 v[162:165], v141 offset:49152
	ds_read_b128 v[166:169], v141 offset:50176
	ds_read_b128 v[170:173], v141 offset:51200
	ds_read_b128 v[190:193], v141 offset:52224
	ds_read_b128 v[194:197], v141 offset:53248
	ds_read_b128 v[198:201], v141 offset:54272
	ds_read_b128 v[202:205], v141 offset:55296
	ds_read_b128 v[206:209], v141 offset:56320
	s_nop 0
	global_load_lds_dwordx4 v0, s[66:67]
	v_mov_b32_e32 v0, v136
	s_mov_b32 m0, s69
	s_nop 0
	global_load_lds_dwordx4 v0, s[66:67]
	s_barrier
	s_waitcnt lgkmcnt(0)
	s_setprio 1
	s_waitcnt lgkmcnt(0)
	v_mfma_f32_16x16x32_bf16 v[56:59], v[146:149], v[162:165], v[56:59]
	v_mfma_f32_16x16x32_bf16 v[52:55], v[154:157], v[162:165], v[52:55]
	v_mfma_f32_16x16x32_bf16 v[40:43], v[146:149], v[170:173], v[40:43]
	v_mfma_f32_16x16x32_bf16 v[36:39], v[154:157], v[170:173], v[36:39]
	v_mfma_f32_16x16x32_bf16 v[24:27], v[146:149], v[194:197], v[24:27]
	v_mfma_f32_16x16x32_bf16 v[20:23], v[154:157], v[194:197], v[20:23]
	v_mfma_f32_16x16x32_bf16 v[12:15], v[146:149], v[202:205], v[12:15]
	v_mfma_f32_16x16x32_bf16 v[8:11], v[154:157], v[202:205], v[8:11]
	v_mfma_f32_16x16x32_bf16 v[56:59], v[150:153], v[166:169], v[56:59]
	v_mfma_f32_16x16x32_bf16 v[52:55], v[158:161], v[166:169], v[52:55]
	v_mfma_f32_16x16x32_bf16 v[40:43], v[150:153], v[190:193], v[40:43]
	v_mfma_f32_16x16x32_bf16 v[36:39], v[158:161], v[190:193], v[36:39]
	v_mfma_f32_16x16x32_bf16 v[24:27], v[150:153], v[198:201], v[24:27]
	v_mfma_f32_16x16x32_bf16 v[20:23], v[158:161], v[198:201], v[20:23]
	v_mfma_f32_16x16x32_bf16 v[12:15], v[150:153], v[206:209], v[12:15]
	v_mfma_f32_16x16x32_bf16 v[8:11], v[158:161], v[206:209], v[8:11]
	s_setprio 0
	s_barrier
	s_add_u32 s24, s24, s6
	s_addc_u32 s25, s25, s7
	v_mov_b32_e32 v0, v135
	s_add_i32 s45, s45, s26
	s_mov_b32 m0, s45
	s_nop 0
	global_load_lds_dwordx4 v0, s[24:25]
	v_mov_b32_e32 v0, v137
	s_add_i32 m0, s45, 0x2000
	s_nop 0
	global_load_lds_dwordx4 v0, s[24:25]
	s_barrier
	s_setprio 1
	v_mfma_f32_16x16x32_bf16 v[64:67], v[210:213], v[162:165], v[64:67]
	v_mfma_f32_16x16x32_bf16 v[60:63], v[218:221], v[162:165], v[60:63]
	v_mfma_f32_16x16x32_bf16 v[48:51], v[210:213], v[170:173], v[48:51]
	v_mfma_f32_16x16x32_bf16 v[44:47], v[218:221], v[170:173], v[44:47]
	v_mfma_f32_16x16x32_bf16 v[32:35], v[210:213], v[194:197], v[32:35]
	v_mfma_f32_16x16x32_bf16 v[28:31], v[218:221], v[194:197], v[28:31]
	v_mfma_f32_16x16x32_bf16 v[16:19], v[210:213], v[202:205], v[16:19]
	v_mfma_f32_16x16x32_bf16 v[4:7], v[218:221], v[202:205], v[4:7]
	v_mfma_f32_16x16x32_bf16 v[64:67], v[214:217], v[166:169], v[64:67]
	v_mfma_f32_16x16x32_bf16 v[60:63], v[222:225], v[166:169], v[60:63]
	v_mfma_f32_16x16x32_bf16 v[48:51], v[214:217], v[190:193], v[48:51]
	v_mfma_f32_16x16x32_bf16 v[44:47], v[222:225], v[190:193], v[44:47]
	v_mfma_f32_16x16x32_bf16 v[32:35], v[214:217], v[198:201], v[32:35]
	v_mfma_f32_16x16x32_bf16 v[28:31], v[222:225], v[198:201], v[28:31]
	v_mfma_f32_16x16x32_bf16 v[16:19], v[214:217], v[206:209], v[16:19]
	v_mfma_f32_16x16x32_bf16 v[4:7], v[222:225], v[206:209], v[4:7]
	s_setprio 0
	s_add_u32 s29, s29, 0x100
	s_addc_u32 s30, s30, 0
	s_cmp_lt_i32 s31, s54
	s_mov_b32 s24, s31
	s_waitcnt vmcnt(6)
	s_barrier
	s_cbranch_scc1 .LBB0_371
	v_readlane_b32 s70, v254, 63
	v_readlane_b32 s71, v255, 0
	s_mul_i32 s81, s3, 24
	s_and_b64 vcc, exec, s[40:41]
	s_cbranch_vccz .LBB0_376
	s_branch .LBB0_377

.LBB0_1242:
	s_add_i32 s51, s64, 2
	s_add_u32 s66, s56, s24
	s_addc_u32 s67, s57, s25
	s_add_i32 s86, 0, 0x10000
	v_add_u32_e32 v0, s86, v163
	s_add_u32 s84, s21, s24
	ds_read_b128 v[132:135], v0
	ds_read_b128 v[136:139], v0 offset:1024
	ds_read_b128 v[140:143], v0 offset:2048
	ds_read_b128 v[146:149], v0 offset:3072
	s_addc_u32 s85, s49, s25
	s_add_u32 s84, s84, 0xffffff80
	s_addc_u32 s85, s85, -1
	s_add_i32 vcc_hi, s86, s17
	s_add_i32 m0, s30, 0xc000
	s_add_i32 s87, s30, 0xe000
	s_add_i32 vcc_lo, 0, 0x14000
	s_add_i32 s89, vcc_hi, 0x2000
	s_cmp_eq_u32 s79, s64
	s_cselect_b32 s64, 0, s25
	s_cselect_b32 s67, s43, s67
	s_cselect_b32 s66, s42, s66
	s_cselect_b32 s14, 0, s24
	v_mov_b32_e32 v0, v160
	ds_read_b128 v[150:153], v165
	ds_read_b128 v[154:157], v165 offset:1024
	ds_read_b128 v[166:169], v165 offset:2048
	ds_read_b128 v[170:173], v165 offset:3072
	ds_read_b128 v[190:193], v165 offset:4096
	ds_read_b128 v[194:197], v165 offset:5120
	ds_read_b128 v[198:201], v165 offset:6144
	ds_read_b128 v[202:205], v165 offset:7168
	s_nop 0
	global_load_lds_dwordx4 v0, s[84:85]
	v_mov_b32_e32 v0, v161
	s_mov_b32 m0, s87
	s_nop 0
	global_load_lds_dwordx4 v0, s[84:85]
	s_waitcnt lgkmcnt(8)
	s_barrier
	s_waitcnt lgkmcnt(0)
	s_setprio 1
	s_waitcnt lgkmcnt(0)
	v_mfma_f32_16x16x32_bf16 v[128:131], v[132:135], v[150:153], v[128:131]
	v_mfma_f32_16x16x32_bf16 v[96:99], v[140:143], v[150:153], v[96:99]
	v_mfma_f32_16x16x32_bf16 v[120:123], v[132:135], v[166:169], v[120:123]
	v_mfma_f32_16x16x32_bf16 v[88:91], v[140:143], v[166:169], v[88:91]
	v_mfma_f32_16x16x32_bf16 v[112:115], v[132:135], v[190:193], v[112:115]
	v_mfma_f32_16x16x32_bf16 v[80:83], v[140:143], v[190:193], v[80:83]
	v_mfma_f32_16x16x32_bf16 v[104:107], v[132:135], v[198:201], v[104:107]
	v_mfma_f32_16x16x32_bf16 v[72:75], v[140:143], v[198:201], v[72:75]
	v_mfma_f32_16x16x32_bf16 v[128:131], v[136:139], v[154:157], v[128:131]
	v_mfma_f32_16x16x32_bf16 v[96:99], v[146:149], v[154:157], v[96:99]
	v_mfma_f32_16x16x32_bf16 v[120:123], v[136:139], v[170:173], v[120:123]
	v_mfma_f32_16x16x32_bf16 v[88:91], v[146:149], v[170:173], v[88:91]
	v_mfma_f32_16x16x32_bf16 v[112:115], v[136:139], v[194:197], v[112:115]
	v_mfma_f32_16x16x32_bf16 v[80:83], v[146:149], v[194:197], v[80:83]
	v_mfma_f32_16x16x32_bf16 v[104:107], v[136:139], v[202:205], v[104:107]
	v_mfma_f32_16x16x32_bf16 v[72:75], v[146:149], v[202:205], v[72:75]
	s_setprio 0
	s_barrier
	v_add_u32_e32 v0, vcc_lo, v163
	ds_read_b128 v[206:209], v0
	ds_read_b128 v[210:213], v0 offset:1024
	ds_read_b128 v[214:217], v0 offset:2048
	ds_read_b128 v[218:221], v0 offset:3072
	s_mov_b64 s[84:85], s[66:67]
	v_mov_b32_e32 v0, v160
	s_mov_b32 m0, vcc_hi
	s_nop 0
	global_load_lds_dwordx4 v0, s[84:85]
	v_mov_b32_e32 v0, v161
	s_mov_b32 m0, s89
	s_nop 0
	global_load_lds_dwordx4 v0, s[84:85]
	s_barrier
	s_waitcnt lgkmcnt(0)
	s_setprio 1
	s_waitcnt lgkmcnt(0)
	v_mfma_f32_16x16x32_bf16 v[64:67], v[206:209], v[150:153], v[64:67]
	v_mfma_f32_16x16x32_bf16 v[32:35], v[214:217], v[150:153], v[32:35]
	v_mfma_f32_16x16x32_bf16 v[56:59], v[206:209], v[166:169], v[56:59]
	v_mfma_f32_16x16x32_bf16 v[24:27], v[214:217], v[166:169], v[24:27]
	v_mfma_f32_16x16x32_bf16 v[48:51], v[206:209], v[190:193], v[48:51]
	v_mfma_f32_16x16x32_bf16 v[16:19], v[214:217], v[190:193], v[16:19]
	v_mfma_f32_16x16x32_bf16 v[40:43], v[206:209], v[198:201], v[40:43]
	v_mfma_f32_16x16x32_bf16 v[8:11], v[214:217], v[198:201], v[8:11]
	v_mfma_f32_16x16x32_bf16 v[64:67], v[210:213], v[154:157], v[64:67]
	v_mfma_f32_16x16x32_bf16 v[32:35], v[218:221], v[154:157], v[32:35]
	v_mfma_f32_16x16x32_bf16 v[56:59], v[210:213], v[170:173], v[56:59]
	v_mfma_f32_16x16x32_bf16 v[24:27], v[218:221], v[170:173], v[24:27]
	v_mfma_f32_16x16x32_bf16 v[48:51], v[210:213], v[194:197], v[48:51]
	v_mfma_f32_16x16x32_bf16 v[16:19], v[218:221], v[194:197], v[16:19]
	v_mfma_f32_16x16x32_bf16 v[40:43], v[210:213], v[202:205], v[40:43]
	v_mfma_f32_16x16x32_bf16 v[8:11], v[218:221], v[202:205], v[8:11]
	s_setprio 0
	s_cselect_b32 s89, s52, s58
	s_cselect_b32 s15, s53, s59
	s_add_u32 s84, s89, s14
	s_addc_u32 s85, s15, s64
	s_mov_b64 s[86:87], s[84:85]
	v_mov_b32_e32 v0, v160
	s_mov_b32 m0, s30
	s_barrier
	ds_read_b128 v[150:153], v165 offset:16384
	ds_read_b128 v[154:157], v165 offset:17408
	ds_read_b128 v[166:169], v165 offset:18432
	ds_read_b128 v[170:173], v165 offset:19456
	ds_read_b128 v[190:193], v165 offset:20480
	ds_read_b128 v[194:197], v165 offset:21504
	ds_read_b128 v[198:201], v165 offset:22528
	ds_read_b128 v[202:205], v165 offset:23552
	s_nop 0
	global_load_lds_dwordx4 v0, s[86:87]
	v_mov_b32_e32 v0, v161
	s_mov_b32 m0, s31
	s_nop 0
	global_load_lds_dwordx4 v0, s[86:87]
	s_barrier
	s_waitcnt lgkmcnt(0)
	s_setprio 1
	s_waitcnt lgkmcnt(0)
	v_mfma_f32_16x16x32_bf16 v[124:127], v[132:135], v[150:153], v[124:127]
	v_mfma_f32_16x16x32_bf16 v[92:95], v[140:143], v[150:153], v[92:95]
	v_mfma_f32_16x16x32_bf16 v[116:119], v[132:135], v[166:169], v[116:119]
	v_mfma_f32_16x16x32_bf16 v[84:87], v[140:143], v[166:169], v[84:87]
	v_mfma_f32_16x16x32_bf16 v[108:111], v[132:135], v[190:193], v[108:111]
	v_mfma_f32_16x16x32_bf16 v[76:79], v[140:143], v[190:193], v[76:79]
	v_mfma_f32_16x16x32_bf16 v[100:103], v[132:135], v[198:201], v[100:103]
	v_mfma_f32_16x16x32_bf16 v[68:71], v[140:143], v[198:201], v[68:71]
	v_mfma_f32_16x16x32_bf16 v[124:127], v[136:139], v[154:157], v[124:127]
	v_mfma_f32_16x16x32_bf16 v[92:95], v[146:149], v[154:157], v[92:95]
	v_mfma_f32_16x16x32_bf16 v[116:119], v[136:139], v[170:173], v[116:119]
	v_mfma_f32_16x16x32_bf16 v[84:87], v[146:149], v[170:173], v[84:87]
	v_mfma_f32_16x16x32_bf16 v[108:111], v[136:139], v[194:197], v[108:111]
	v_mfma_f32_16x16x32_bf16 v[76:79], v[146:149], v[194:197], v[76:79]
	v_mfma_f32_16x16x32_bf16 v[100:103], v[136:139], v[202:205], v[100:103]
	v_mfma_f32_16x16x32_bf16 v[68:71], v[146:149], v[202:205], v[68:71]
	s_setprio 0
	s_barrier
	s_add_u32 s86, s66, s44
	s_addc_u32 s87, s67, s45
	v_mov_b32_e32 v0, v160
	s_add_i32 vcc_lo, vcc_lo, s17
	s_mov_b32 m0, vcc_lo
	s_nop 0
	global_load_lds_dwordx4 v0, s[86:87]
	v_mov_b32_e32 v0, v161
	s_add_i32 m0, vcc_lo, 0x2000
	s_nop 0
	global_load_lds_dwordx4 v0, s[86:87]
	s_barrier
	s_setprio 1
	v_mfma_f32_16x16x32_bf16 v[60:63], v[206:209], v[150:153], v[60:63]
	v_mfma_f32_16x16x32_bf16 v[28:31], v[214:217], v[150:153], v[28:31]
	v_mfma_f32_16x16x32_bf16 v[52:55], v[206:209], v[166:169], v[52:55]
	v_mfma_f32_16x16x32_bf16 v[20:23], v[214:217], v[166:169], v[20:23]
	v_mfma_f32_16x16x32_bf16 v[44:47], v[206:209], v[190:193], v[44:47]
	v_mfma_f32_16x16x32_bf16 v[12:15], v[214:217], v[190:193], v[12:15]
	v_mfma_f32_16x16x32_bf16 v[36:39], v[206:209], v[198:201], v[36:39]
	v_mfma_f32_16x16x32_bf16 v[4:7], v[214:217], v[198:201], v[4:7]
	v_mfma_f32_16x16x32_bf16 v[60:63], v[210:213], v[154:157], v[60:63]
	v_mfma_f32_16x16x32_bf16 v[28:31], v[218:221], v[154:157], v[28:31]
	v_mfma_f32_16x16x32_bf16 v[52:55], v[210:213], v[170:173], v[52:55]
	v_mfma_f32_16x16x32_bf16 v[20:23], v[218:221], v[170:173], v[20:23]
	v_mfma_f32_16x16x32_bf16 v[44:47], v[210:213], v[194:197], v[44:47]
	v_mfma_f32_16x16x32_bf16 v[12:15], v[218:221], v[194:197], v[12:15]
	v_mfma_f32_16x16x32_bf16 v[36:39], v[210:213], v[202:205], v[36:39]
	v_mfma_f32_16x16x32_bf16 v[4:7], v[218:221], v[202:205], v[4:7]
	s_setprio 0
	s_add_i32 vcc_lo, 0, 0x18000
	v_add_u32_e32 v0, vcc_lo, v163
	s_waitcnt vmcnt(6)
	s_barrier
	ds_read_b128 v[132:135], v0
	ds_read_b128 v[136:139], v0 offset:1024
	ds_read_b128 v[140:143], v0 offset:2048
	ds_read_b128 v[146:149], v0 offset:3072
	s_add_u32 s86, s89, s44
	s_addc_u32 s15, s15, s45
	s_add_u32 s86, s86, s14
	s_addc_u32 s87, s15, s64
	v_mov_b32_e32 v0, v160
	s_mov_b32 m0, s55
	ds_read_b128 v[150:153], v165 offset:32768
	ds_read_b128 v[154:157], v165 offset:33792
	ds_read_b128 v[166:169], v165 offset:34816
	ds_read_b128 v[170:173], v165 offset:35840
	ds_read_b128 v[190:193], v165 offset:36864
	ds_read_b128 v[194:197], v165 offset:37888
	ds_read_b128 v[198:201], v165 offset:38912
	ds_read_b128 v[202:205], v165 offset:39936
	s_nop 0
	global_load_lds_dwordx4 v0, s[86:87]
	v_mov_b32_e32 v0, v161
	s_mov_b32 m0, s69
	s_nop 0
	global_load_lds_dwordx4 v0, s[86:87]
	s_waitcnt lgkmcnt(8)
	s_barrier
	s_waitcnt lgkmcnt(0)
	s_setprio 1
	s_waitcnt lgkmcnt(0)
	v_mfma_f32_16x16x32_bf16 v[128:131], v[132:135], v[150:153], v[128:131]
	v_mfma_f32_16x16x32_bf16 v[96:99], v[140:143], v[150:153], v[96:99]
	v_mfma_f32_16x16x32_bf16 v[120:123], v[132:135], v[166:169], v[120:123]
	v_mfma_f32_16x16x32_bf16 v[88:91], v[140:143], v[166:169], v[88:91]
	v_mfma_f32_16x16x32_bf16 v[112:115], v[132:135], v[190:193], v[112:115]
	v_mfma_f32_16x16x32_bf16 v[80:83], v[140:143], v[190:193], v[80:83]
	v_mfma_f32_16x16x32_bf16 v[104:107], v[132:135], v[198:201], v[104:107]
	v_mfma_f32_16x16x32_bf16 v[72:75], v[140:143], v[198:201], v[72:75]
	v_mfma_f32_16x16x32_bf16 v[128:131], v[136:139], v[154:157], v[128:131]
	v_mfma_f32_16x16x32_bf16 v[96:99], v[146:149], v[154:157], v[96:99]
	v_mfma_f32_16x16x32_bf16 v[120:123], v[136:139], v[170:173], v[120:123]
	v_mfma_f32_16x16x32_bf16 v[88:91], v[146:149], v[170:173], v[88:91]
	v_mfma_f32_16x16x32_bf16 v[112:115], v[136:139], v[194:197], v[112:115]
	v_mfma_f32_16x16x32_bf16 v[80:83], v[146:149], v[194:197], v[80:83]
	v_mfma_f32_16x16x32_bf16 v[104:107], v[136:139], v[202:205], v[104:107]
	v_mfma_f32_16x16x32_bf16 v[72:75], v[146:149], v[202:205], v[72:75]
	s_setprio 0
	s_barrier
	s_add_i32 s14, 0, 0x1c000
	s_add_u32 s66, s66, 0x80
	v_add_u32_e32 v0, s14, v163
	s_addc_u32 s67, s67, 0
	ds_read_b128 v[206:209], v0
	ds_read_b128 v[210:213], v0 offset:1024
	ds_read_b128 v[214:217], v0 offset:2048
	ds_read_b128 v[218:221], v0 offset:3072
	s_mov_b64 s[86:87], s[66:67]
	v_mov_b32_e32 v0, v160
	s_add_i32 s15, vcc_lo, s17
	s_mov_b32 m0, s15
	s_nop 0
	global_load_lds_dwordx4 v0, s[86:87]
	v_mov_b32_e32 v0, v161
	s_add_i32 m0, s15, 0x2000
	s_nop 0
	global_load_lds_dwordx4 v0, s[86:87]
	s_barrier
	s_waitcnt lgkmcnt(0)
	s_setprio 1
	s_waitcnt lgkmcnt(0)
	v_mfma_f32_16x16x32_bf16 v[64:67], v[206:209], v[150:153], v[64:67]
	v_mfma_f32_16x16x32_bf16 v[32:35], v[214:217], v[150:153], v[32:35]
	v_mfma_f32_16x16x32_bf16 v[56:59], v[206:209], v[166:169], v[56:59]
	v_mfma_f32_16x16x32_bf16 v[24:27], v[214:217], v[166:169], v[24:27]
	v_mfma_f32_16x16x32_bf16 v[48:51], v[206:209], v[190:193], v[48:51]
	v_mfma_f32_16x16x32_bf16 v[16:19], v[214:217], v[190:193], v[16:19]
	v_mfma_f32_16x16x32_bf16 v[40:43], v[206:209], v[198:201], v[40:43]
	v_mfma_f32_16x16x32_bf16 v[8:11], v[214:217], v[198:201], v[8:11]
	v_mfma_f32_16x16x32_bf16 v[64:67], v[210:213], v[154:157], v[64:67]
	v_mfma_f32_16x16x32_bf16 v[32:35], v[218:221], v[154:157], v[32:35]
	v_mfma_f32_16x16x32_bf16 v[56:59], v[210:213], v[170:173], v[56:59]
	v_mfma_f32_16x16x32_bf16 v[24:27], v[218:221], v[170:173], v[24:27]
	v_mfma_f32_16x16x32_bf16 v[48:51], v[210:213], v[194:197], v[48:51]
	v_mfma_f32_16x16x32_bf16 v[16:19], v[218:221], v[194:197], v[16:19]
	v_mfma_f32_16x16x32_bf16 v[40:43], v[210:213], v[202:205], v[40:43]
	v_mfma_f32_16x16x32_bf16 v[8:11], v[218:221], v[202:205], v[8:11]
	s_setprio 0
	s_add_u32 s84, s84, 0x80
	s_addc_u32 s85, s85, 0
	v_mov_b32_e32 v0, v160
	s_mov_b32 m0, s71
	s_barrier
	ds_read_b128 v[150:153], v165 offset:49152
	ds_read_b128 v[154:157], v165 offset:50176
	ds_read_b128 v[166:169], v165 offset:51200
	ds_read_b128 v[170:173], v165 offset:52224
	ds_read_b128 v[190:193], v165 offset:53248
	ds_read_b128 v[194:197], v165 offset:54272
	ds_read_b128 v[198:201], v165 offset:55296
	ds_read_b128 v[202:205], v165 offset:56320
	s_nop 0
	global_load_lds_dwordx4 v0, s[84:85]
	v_mov_b32_e32 v0, v161
	s_mov_b32 m0, s75
	s_nop 0
	global_load_lds_dwordx4 v0, s[84:85]
	s_barrier
	s_waitcnt lgkmcnt(0)
	s_setprio 1
	s_waitcnt lgkmcnt(0)
	v_mfma_f32_16x16x32_bf16 v[124:127], v[132:135], v[150:153], v[124:127]
	v_mfma_f32_16x16x32_bf16 v[92:95], v[140:143], v[150:153], v[92:95]
	v_mfma_f32_16x16x32_bf16 v[116:119], v[132:135], v[166:169], v[116:119]
	v_mfma_f32_16x16x32_bf16 v[84:87], v[140:143], v[166:169], v[84:87]
	v_mfma_f32_16x16x32_bf16 v[108:111], v[132:135], v[190:193], v[108:111]
	v_mfma_f32_16x16x32_bf16 v[76:79], v[140:143], v[190:193], v[76:79]
	v_mfma_f32_16x16x32_bf16 v[100:103], v[132:135], v[198:201], v[100:103]
	v_mfma_f32_16x16x32_bf16 v[68:71], v[140:143], v[198:201], v[68:71]
	v_mfma_f32_16x16x32_bf16 v[124:127], v[136:139], v[154:157], v[124:127]
	v_mfma_f32_16x16x32_bf16 v[92:95], v[146:149], v[154:157], v[92:95]
	v_mfma_f32_16x16x32_bf16 v[116:119], v[136:139], v[170:173], v[116:119]
	v_mfma_f32_16x16x32_bf16 v[84:87], v[146:149], v[170:173], v[84:87]
	v_mfma_f32_16x16x32_bf16 v[108:111], v[136:139], v[194:197], v[108:111]
	v_mfma_f32_16x16x32_bf16 v[76:79], v[146:149], v[194:197], v[76:79]
	v_mfma_f32_16x16x32_bf16 v[100:103], v[136:139], v[202:205], v[100:103]
	v_mfma_f32_16x16x32_bf16 v[68:71], v[146:149], v[202:205], v[68:71]
	s_setprio 0
	s_barrier
	s_add_u32 s66, s66, s44
	s_addc_u32 s67, s67, s45
	v_mov_b32_e32 v0, v160
	s_add_i32 s14, s14, s17
	s_mov_b32 m0, s14
	s_nop 0
	global_load_lds_dwordx4 v0, s[66:67]
	v_mov_b32_e32 v0, v161
	s_add_i32 m0, s14, 0x2000
	s_nop 0
	global_load_lds_dwordx4 v0, s[66:67]
	s_barrier
	s_setprio 1
	v_mfma_f32_16x16x32_bf16 v[60:63], v[206:209], v[150:153], v[60:63]
	v_mfma_f32_16x16x32_bf16 v[28:31], v[214:217], v[150:153], v[28:31]
	v_mfma_f32_16x16x32_bf16 v[52:55], v[206:209], v[166:169], v[52:55]
	v_mfma_f32_16x16x32_bf16 v[20:23], v[214:217], v[166:169], v[20:23]
	v_mfma_f32_16x16x32_bf16 v[44:47], v[206:209], v[190:193], v[44:47]
	v_mfma_f32_16x16x32_bf16 v[12:15], v[214:217], v[190:193], v[12:15]
	v_mfma_f32_16x16x32_bf16 v[36:39], v[206:209], v[198:201], v[36:39]
	v_mfma_f32_16x16x32_bf16 v[4:7], v[214:217], v[198:201], v[4:7]
	v_mfma_f32_16x16x32_bf16 v[60:63], v[210:213], v[154:157], v[60:63]
	v_mfma_f32_16x16x32_bf16 v[28:31], v[218:221], v[154:157], v[28:31]
	v_mfma_f32_16x16x32_bf16 v[52:55], v[210:213], v[170:173], v[52:55]
	v_mfma_f32_16x16x32_bf16 v[20:23], v[218:221], v[170:173], v[20:23]
	v_mfma_f32_16x16x32_bf16 v[44:47], v[210:213], v[194:197], v[44:47]
	v_mfma_f32_16x16x32_bf16 v[12:15], v[218:221], v[194:197], v[12:15]
	v_mfma_f32_16x16x32_bf16 v[36:39], v[210:213], v[202:205], v[36:39]
	v_mfma_f32_16x16x32_bf16 v[4:7], v[218:221], v[202:205], v[4:7]
	s_setprio 0
	s_add_u32 s24, s24, 0x100
	s_addc_u32 s25, s25, 0
	s_cmp_lt_i32 s51, s70
	s_mov_b32 s64, s51
	s_waitcnt vmcnt(6)
	s_barrier
	s_cbranch_scc1 .LBB0_1242
	s_mov_b32 s89, s18
	s_mov_b32 s19, s68
	s_mov_b32 s68, s22
	s_mov_b32 s18, s23
	s_mov_b32 s23, s38
	v_readlane_b32 s38, v254, 62

.LBB0_1556:
	s_cmp_eq_u32 s58, s10
	s_cselect_b64 vcc, -1, 0
	s_add_i32 s10, s10, 2
	s_add_u32 s14, s4, s20
	s_addc_u32 s15, s5, s21
	s_and_b64 s[24:25], vcc, exec
	s_cselect_b32 s25, s45, s15
	s_cselect_b32 s24, s44, s14
	s_add_i32 s14, 0, 0x10000
	v_add_u32_e32 v0, s14, v150
	s_waitcnt lgkmcnt(0)
	ds_read_b128 v[132:135], v0
	ds_read_b128 v[158:161], v0 offset:1024
	ds_read_b128 v[162:165], v0 offset:2048
	ds_read_b128 v[166:169], v0 offset:3072
	s_and_b64 s[30:31], vcc, exec
	s_cselect_b32 s15, 0, s21
	s_cselect_b32 s29, 0, s20
	s_add_u32 s30, s76, s20
	s_addc_u32 s31, s77, s21
	s_add_u32 s30, s30, 0xffffff80
	s_addc_u32 s31, s31, -1
	v_mov_b32_e32 v0, v146
	ds_read_b128 v[170:173], v152
	ds_read_b128 v[190:193], v152 offset:1024
	ds_read_b128 v[194:197], v152 offset:2048
	ds_read_b128 v[198:201], v152 offset:3072
	ds_read_b128 v[202:205], v152 offset:4096
	ds_read_b128 v[206:209], v152 offset:5120
	ds_read_b128 v[210:213], v152 offset:6144
	ds_read_b128 v[214:217], v152 offset:7168
	s_add_i32 m0, s27, 0xc000
	s_nop 0
	global_load_lds_dwordx4 v0, s[30:31]
	v_mov_b32_e32 v0, v148
	s_add_i32 m0, s27, 0xe000
	s_nop 0
	global_load_lds_dwordx4 v0, s[30:31]
	s_waitcnt lgkmcnt(8)
	s_barrier
	s_waitcnt lgkmcnt(0)
	s_setprio 1
	s_waitcnt lgkmcnt(0)
	v_mfma_f32_16x16x32_bf16 v[4:7], v[132:135], v[170:173], v[4:7]
	v_mfma_f32_16x16x32_bf16 v[8:11], v[162:165], v[170:173], v[8:11]
	v_mfma_f32_16x16x32_bf16 v[12:15], v[132:135], v[194:197], v[12:15]
	v_mfma_f32_16x16x32_bf16 v[16:19], v[162:165], v[194:197], v[16:19]
	v_mfma_f32_16x16x32_bf16 v[20:23], v[132:135], v[202:205], v[20:23]
	v_mfma_f32_16x16x32_bf16 v[24:27], v[162:165], v[202:205], v[24:27]
	v_mfma_f32_16x16x32_bf16 v[28:31], v[132:135], v[210:213], v[28:31]
	v_mfma_f32_16x16x32_bf16 v[32:35], v[162:165], v[210:213], v[32:35]
	v_mfma_f32_16x16x32_bf16 v[4:7], v[158:161], v[190:193], v[4:7]
	v_mfma_f32_16x16x32_bf16 v[8:11], v[166:169], v[190:193], v[8:11]
	v_mfma_f32_16x16x32_bf16 v[12:15], v[158:161], v[198:201], v[12:15]
	v_mfma_f32_16x16x32_bf16 v[16:19], v[166:169], v[198:201], v[16:19]
	v_mfma_f32_16x16x32_bf16 v[20:23], v[158:161], v[206:209], v[20:23]
	v_mfma_f32_16x16x32_bf16 v[24:27], v[166:169], v[206:209], v[24:27]
	v_mfma_f32_16x16x32_bf16 v[28:31], v[158:161], v[214:217], v[28:31]
	v_mfma_f32_16x16x32_bf16 v[32:35], v[166:169], v[214:217], v[32:35]
	s_setprio 0
	s_barrier
	s_add_i32 s47, 0, 0x14000
	v_add_u32_e32 v0, s47, v150
	ds_read_b128 v[218:221], v0
	ds_read_b128 v[222:225], v0 offset:1024
	ds_read_b128 v[226:229], v0 offset:2048
	ds_read_b128 v[230:233], v0 offset:3072
	s_mov_b64 s[30:31], s[24:25]
	v_mov_b32_e32 v0, v142
	s_add_i32 s14, s14, s26
	s_mov_b32 m0, s14
	s_nop 0
	global_load_lds_dwordx4 v0, s[30:31]
	v_mov_b32_e32 v0, v143
	s_add_i32 m0, s14, 0x2000
	s_nop 0
	global_load_lds_dwordx4 v0, s[30:31]
	s_barrier
	s_waitcnt lgkmcnt(0)
	s_setprio 1
	s_waitcnt lgkmcnt(0)
	v_mfma_f32_16x16x32_bf16 v[40:43], v[218:221], v[170:173], v[40:43]
	v_mfma_f32_16x16x32_bf16 v[44:47], v[226:229], v[170:173], v[44:47]
	v_mfma_f32_16x16x32_bf16 v[48:51], v[218:221], v[194:197], v[48:51]
	v_mfma_f32_16x16x32_bf16 v[52:55], v[226:229], v[194:197], v[52:55]
	v_mfma_f32_16x16x32_bf16 v[56:59], v[218:221], v[202:205], v[56:59]
	v_mfma_f32_16x16x32_bf16 v[60:63], v[226:229], v[202:205], v[60:63]
	v_mfma_f32_16x16x32_bf16 v[68:71], v[218:221], v[210:213], v[68:71]
	v_mfma_f32_16x16x32_bf16 v[76:79], v[226:229], v[210:213], v[76:79]
	v_mfma_f32_16x16x32_bf16 v[40:43], v[222:225], v[190:193], v[40:43]
	v_mfma_f32_16x16x32_bf16 v[44:47], v[230:233], v[190:193], v[44:47]
	v_mfma_f32_16x16x32_bf16 v[48:51], v[222:225], v[198:201], v[48:51]
	v_mfma_f32_16x16x32_bf16 v[52:55], v[230:233], v[198:201], v[52:55]
	v_mfma_f32_16x16x32_bf16 v[56:59], v[222:225], v[206:209], v[56:59]
	v_mfma_f32_16x16x32_bf16 v[60:63], v[230:233], v[206:209], v[60:63]
	v_mfma_f32_16x16x32_bf16 v[68:71], v[222:225], v[214:217], v[68:71]
	v_mfma_f32_16x16x32_bf16 v[76:79], v[230:233], v[214:217], v[76:79]
	s_setprio 0
	s_add_u32 s50, s76, s29
	v_cndmask_b32_e32 v0, v147, v153, vcc
	s_addc_u32 s51, s77, s15
	s_mov_b64 s[30:31], s[50:51]
	v_mov_b32_e32 v157, v0
	s_mov_b32 m0, s27
	s_barrier
	ds_read_b128 v[170:173], v152 offset:16384
	ds_read_b128 v[190:193], v152 offset:17408
	ds_read_b128 v[194:197], v152 offset:18432
	ds_read_b128 v[198:201], v152 offset:19456
	ds_read_b128 v[202:205], v152 offset:20480
	ds_read_b128 v[206:209], v152 offset:21504
	ds_read_b128 v[210:213], v152 offset:22528
	ds_read_b128 v[214:217], v152 offset:23552
	v_cndmask_b32_e32 v1, v145, v154, vcc
	s_nop 0
	global_load_lds_dwordx4 v157, s[30:31]
	v_mov_b32_e32 v157, v1
	s_mov_b32 m0, s52
	s_nop 0
	global_load_lds_dwordx4 v157, s[30:31]
	s_barrier
	s_waitcnt lgkmcnt(0)
	s_setprio 1
	s_waitcnt lgkmcnt(0)
	v_mfma_f32_16x16x32_bf16 v[64:67], v[132:135], v[170:173], v[64:67]
	v_mfma_f32_16x16x32_bf16 v[72:75], v[162:165], v[170:173], v[72:75]
	v_mfma_f32_16x16x32_bf16 v[80:83], v[132:135], v[194:197], v[80:83]
	v_mfma_f32_16x16x32_bf16 v[84:87], v[162:165], v[194:197], v[84:87]
	v_mfma_f32_16x16x32_bf16 v[88:91], v[132:135], v[202:205], v[88:91]
	v_mfma_f32_16x16x32_bf16 v[92:95], v[162:165], v[202:205], v[92:95]
	v_mfma_f32_16x16x32_bf16 v[96:99], v[132:135], v[210:213], v[96:99]
	v_mfma_f32_16x16x32_bf16 v[100:103], v[162:165], v[210:213], v[100:103]
	v_mfma_f32_16x16x32_bf16 v[64:67], v[158:161], v[190:193], v[64:67]
	v_mfma_f32_16x16x32_bf16 v[72:75], v[166:169], v[190:193], v[72:75]
	v_mfma_f32_16x16x32_bf16 v[80:83], v[158:161], v[198:201], v[80:83]
	v_mfma_f32_16x16x32_bf16 v[84:87], v[166:169], v[198:201], v[84:87]
	v_mfma_f32_16x16x32_bf16 v[88:91], v[158:161], v[206:209], v[88:91]
	v_mfma_f32_16x16x32_bf16 v[92:95], v[166:169], v[206:209], v[92:95]
	v_mfma_f32_16x16x32_bf16 v[96:99], v[158:161], v[214:217], v[96:99]
	v_mfma_f32_16x16x32_bf16 v[100:103], v[166:169], v[214:217], v[100:103]
	s_setprio 0
	s_barrier
	s_add_u32 s30, s24, s0
	s_addc_u32 s31, s25, s1
	v_mov_b32_e32 v132, v142
	s_add_i32 s14, s47, s26
	s_mov_b32 m0, s14
	s_nop 0
	global_load_lds_dwordx4 v132, s[30:31]
	v_mov_b32_e32 v132, v143
	s_add_i32 m0, s14, 0x2000
	s_nop 0
	global_load_lds_dwordx4 v132, s[30:31]
	s_barrier
	s_setprio 1
	v_mfma_f32_16x16x32_bf16 v[104:107], v[218:221], v[170:173], v[104:107]
	v_mfma_f32_16x16x32_bf16 v[108:111], v[226:229], v[170:173], v[108:111]
	v_mfma_f32_16x16x32_bf16 v[112:115], v[218:221], v[194:197], v[112:115]
	v_mfma_f32_16x16x32_bf16 v[116:119], v[226:229], v[194:197], v[116:119]
	v_mfma_f32_16x16x32_bf16 v[120:123], v[218:221], v[202:205], v[120:123]
	v_mfma_f32_16x16x32_bf16 v[124:127], v[226:229], v[202:205], v[124:127]
	v_mfma_f32_16x16x32_bf16 v[128:131], v[218:221], v[210:213], v[128:131]
	v_mfma_f32_16x16x32_bf16 v[36:39], v[226:229], v[210:213], v[36:39]
	v_mfma_f32_16x16x32_bf16 v[104:107], v[222:225], v[190:193], v[104:107]
	v_mfma_f32_16x16x32_bf16 v[108:111], v[230:233], v[190:193], v[108:111]
	v_mfma_f32_16x16x32_bf16 v[112:115], v[222:225], v[198:201], v[112:115]
	v_mfma_f32_16x16x32_bf16 v[116:119], v[230:233], v[198:201], v[116:119]
	v_mfma_f32_16x16x32_bf16 v[120:123], v[222:225], v[206:209], v[120:123]
	v_mfma_f32_16x16x32_bf16 v[124:127], v[230:233], v[206:209], v[124:127]
	v_mfma_f32_16x16x32_bf16 v[128:131], v[222:225], v[214:217], v[128:131]
	v_mfma_f32_16x16x32_bf16 v[36:39], v[230:233], v[214:217], v[36:39]
	s_setprio 0
	s_add_i32 s14, 0, 0x18000
	v_add_u32_e32 v157, s14, v150
	s_waitcnt vmcnt(6)
	s_barrier
	ds_read_b128 v[132:135], v157
	ds_read_b128 v[158:161], v157 offset:1024
	ds_read_b128 v[162:165], v157 offset:2048
	ds_read_b128 v[166:169], v157 offset:3072
	s_mov_b32 m0, s53
	v_cndmask_b32_e32 v157, v146, v155, vcc
	s_mov_b64 s[30:31], s[50:51]
	ds_read_b128 v[170:173], v152 offset:32768
	ds_read_b128 v[190:193], v152 offset:33792
	ds_read_b128 v[194:197], v152 offset:34816
	ds_read_b128 v[198:201], v152 offset:35840
	ds_read_b128 v[202:205], v152 offset:36864
	ds_read_b128 v[206:209], v152 offset:37888
	ds_read_b128 v[210:213], v152 offset:38912
	ds_read_b128 v[214:217], v152 offset:39936
	v_cndmask_b32_e32 v182, v148, v156, vcc
	s_nop 0
	global_load_lds_dwordx4 v157, s[30:31]
	s_mov_b32 m0, s54
	s_nop 0
	global_load_lds_dwordx4 v182, s[30:31]
	s_waitcnt lgkmcnt(8)
	s_barrier
	s_waitcnt lgkmcnt(0)
	s_setprio 1
	s_waitcnt lgkmcnt(0)
	v_mfma_f32_16x16x32_bf16 v[4:7], v[132:135], v[170:173], v[4:7]
	v_mfma_f32_16x16x32_bf16 v[8:11], v[162:165], v[170:173], v[8:11]
	v_mfma_f32_16x16x32_bf16 v[12:15], v[132:135], v[194:197], v[12:15]
	v_mfma_f32_16x16x32_bf16 v[16:19], v[162:165], v[194:197], v[16:19]
	v_mfma_f32_16x16x32_bf16 v[20:23], v[132:135], v[202:205], v[20:23]
	v_mfma_f32_16x16x32_bf16 v[24:27], v[162:165], v[202:205], v[24:27]
	v_mfma_f32_16x16x32_bf16 v[28:31], v[132:135], v[210:213], v[28:31]
	v_mfma_f32_16x16x32_bf16 v[32:35], v[162:165], v[210:213], v[32:35]
	v_mfma_f32_16x16x32_bf16 v[4:7], v[158:161], v[190:193], v[4:7]
	v_mfma_f32_16x16x32_bf16 v[8:11], v[166:169], v[190:193], v[8:11]
	v_mfma_f32_16x16x32_bf16 v[12:15], v[158:161], v[198:201], v[12:15]
	v_mfma_f32_16x16x32_bf16 v[16:19], v[166:169], v[198:201], v[16:19]
	v_mfma_f32_16x16x32_bf16 v[20:23], v[158:161], v[206:209], v[20:23]
	v_mfma_f32_16x16x32_bf16 v[24:27], v[166:169], v[206:209], v[24:27]
	v_mfma_f32_16x16x32_bf16 v[28:31], v[158:161], v[214:217], v[28:31]
	v_mfma_f32_16x16x32_bf16 v[32:35], v[166:169], v[214:217], v[32:35]
	s_setprio 0
	s_barrier
	s_add_i32 s15, 0, 0x1c000
	s_add_u32 s24, s24, 0x80
	v_add_u32_e32 v157, s15, v150
	s_addc_u32 s25, s25, 0
	ds_read_b128 v[218:221], v157
	ds_read_b128 v[222:225], v157 offset:1024
	ds_read_b128 v[226:229], v157 offset:2048
	ds_read_b128 v[230:233], v157 offset:3072
	s_mov_b64 s[30:31], s[24:25]
	v_mov_b32_e32 v157, v142
	s_add_i32 s14, s14, s26
	s_mov_b32 m0, s14
	s_nop 0
	global_load_lds_dwordx4 v157, s[30:31]
	v_mov_b32_e32 v157, v143
	s_add_i32 m0, s14, 0x2000
	s_nop 0
	global_load_lds_dwordx4 v157, s[30:31]
	s_barrier
	s_waitcnt lgkmcnt(0)
	s_setprio 1
	s_waitcnt lgkmcnt(0)
	v_mfma_f32_16x16x32_bf16 v[40:43], v[218:221], v[170:173], v[40:43]
	v_mfma_f32_16x16x32_bf16 v[44:47], v[226:229], v[170:173], v[44:47]
	v_mfma_f32_16x16x32_bf16 v[48:51], v[218:221], v[194:197], v[48:51]
	v_mfma_f32_16x16x32_bf16 v[52:55], v[226:229], v[194:197], v[52:55]
	v_mfma_f32_16x16x32_bf16 v[56:59], v[218:221], v[202:205], v[56:59]
	v_mfma_f32_16x16x32_bf16 v[60:63], v[226:229], v[202:205], v[60:63]
	v_mfma_f32_16x16x32_bf16 v[68:71], v[218:221], v[210:213], v[68:71]
	v_mfma_f32_16x16x32_bf16 v[76:79], v[226:229], v[210:213], v[76:79]
	v_mfma_f32_16x16x32_bf16 v[40:43], v[222:225], v[190:193], v[40:43]
	v_mfma_f32_16x16x32_bf16 v[44:47], v[230:233], v[190:193], v[44:47]
	v_mfma_f32_16x16x32_bf16 v[48:51], v[222:225], v[198:201], v[48:51]
	v_mfma_f32_16x16x32_bf16 v[52:55], v[230:233], v[198:201], v[52:55]
	v_mfma_f32_16x16x32_bf16 v[56:59], v[222:225], v[206:209], v[56:59]
	v_mfma_f32_16x16x32_bf16 v[60:63], v[230:233], v[206:209], v[60:63]
	v_mfma_f32_16x16x32_bf16 v[68:71], v[222:225], v[214:217], v[68:71]
	v_mfma_f32_16x16x32_bf16 v[76:79], v[230:233], v[214:217], v[76:79]
	s_setprio 0
	s_add_u32 s30, s50, 0x80
	s_addc_u32 s31, s51, 0
	s_mov_b32 m0, s56
	s_barrier
	ds_read_b128 v[170:173], v152 offset:49152
	ds_read_b128 v[190:193], v152 offset:50176
	ds_read_b128 v[194:197], v152 offset:51200
	ds_read_b128 v[198:201], v152 offset:52224
	ds_read_b128 v[202:205], v152 offset:53248
	ds_read_b128 v[206:209], v152 offset:54272
	ds_read_b128 v[210:213], v152 offset:55296
	ds_read_b128 v[214:217], v152 offset:56320
	s_nop 0
	global_load_lds_dwordx4 v0, s[30:31]
	s_mov_b32 m0, s57
	s_nop 0
	global_load_lds_dwordx4 v1, s[30:31]
	s_barrier
	s_waitcnt lgkmcnt(0)
	s_setprio 1
	s_waitcnt lgkmcnt(0)
	v_mfma_f32_16x16x32_bf16 v[64:67], v[132:135], v[170:173], v[64:67]
	v_mfma_f32_16x16x32_bf16 v[72:75], v[162:165], v[170:173], v[72:75]
	v_mfma_f32_16x16x32_bf16 v[80:83], v[132:135], v[194:197], v[80:83]
	v_mfma_f32_16x16x32_bf16 v[84:87], v[162:165], v[194:197], v[84:87]
	v_mfma_f32_16x16x32_bf16 v[88:91], v[132:135], v[202:205], v[88:91]
	v_mfma_f32_16x16x32_bf16 v[92:95], v[162:165], v[202:205], v[92:95]
	v_mfma_f32_16x16x32_bf16 v[96:99], v[132:135], v[210:213], v[96:99]
	v_mfma_f32_16x16x32_bf16 v[100:103], v[162:165], v[210:213], v[100:103]
	v_mfma_f32_16x16x32_bf16 v[64:67], v[158:161], v[190:193], v[64:67]
	v_mfma_f32_16x16x32_bf16 v[72:75], v[166:169], v[190:193], v[72:75]
	v_mfma_f32_16x16x32_bf16 v[80:83], v[158:161], v[198:201], v[80:83]
	v_mfma_f32_16x16x32_bf16 v[84:87], v[166:169], v[198:201], v[84:87]
	v_mfma_f32_16x16x32_bf16 v[88:91], v[158:161], v[206:209], v[88:91]
	v_mfma_f32_16x16x32_bf16 v[92:95], v[166:169], v[206:209], v[92:95]
	v_mfma_f32_16x16x32_bf16 v[96:99], v[158:161], v[214:217], v[96:99]
	v_mfma_f32_16x16x32_bf16 v[100:103], v[166:169], v[214:217], v[100:103]
	s_setprio 0
	s_barrier
	s_add_u32 s24, s24, s0
	s_addc_u32 s25, s25, s1
	v_mov_b32_e32 v0, v142
	s_add_i32 s14, s15, s26
	s_mov_b32 m0, s14
	s_nop 0
	global_load_lds_dwordx4 v0, s[24:25]
	v_mov_b32_e32 v0, v143
	s_add_i32 m0, s14, 0x2000
	s_nop 0
	global_load_lds_dwordx4 v0, s[24:25]
	s_barrier
	s_setprio 1
	v_mfma_f32_16x16x32_bf16 v[104:107], v[218:221], v[170:173], v[104:107]
	v_mfma_f32_16x16x32_bf16 v[108:111], v[226:229], v[170:173], v[108:111]
	v_mfma_f32_16x16x32_bf16 v[112:115], v[218:221], v[194:197], v[112:115]
	v_mfma_f32_16x16x32_bf16 v[116:119], v[226:229], v[194:197], v[116:119]
	v_mfma_f32_16x16x32_bf16 v[120:123], v[218:221], v[202:205], v[120:123]
	v_mfma_f32_16x16x32_bf16 v[124:127], v[226:229], v[202:205], v[124:127]
	v_mfma_f32_16x16x32_bf16 v[128:131], v[218:221], v[210:213], v[128:131]
	v_mfma_f32_16x16x32_bf16 v[36:39], v[226:229], v[210:213], v[36:39]
	v_mfma_f32_16x16x32_bf16 v[104:107], v[222:225], v[190:193], v[104:107]
	v_mfma_f32_16x16x32_bf16 v[108:111], v[230:233], v[190:193], v[108:111]
	v_mfma_f32_16x16x32_bf16 v[112:115], v[222:225], v[198:201], v[112:115]
	v_mfma_f32_16x16x32_bf16 v[116:119], v[230:233], v[198:201], v[116:119]
	v_mfma_f32_16x16x32_bf16 v[120:123], v[222:225], v[206:209], v[120:123]
	v_mfma_f32_16x16x32_bf16 v[124:127], v[230:233], v[206:209], v[124:127]
	v_mfma_f32_16x16x32_bf16 v[128:131], v[222:225], v[214:217], v[128:131]
	v_mfma_f32_16x16x32_bf16 v[36:39], v[230:233], v[214:217], v[36:39]
	s_setprio 0
	s_add_u32 s20, s20, 0x100
	s_addc_u32 s21, s21, 0
	s_cmp_lt_i32 s10, s55
	s_waitcnt vmcnt(6)
	s_barrier
	s_cbranch_scc1 .LBB0_1556

.LBB0_1628:
	s_add_i32 s31, s24, 2
	s_add_u32 s14, s46, s29
	s_addc_u32 s15, s47, s30
	s_add_i32 s25, 0, 0x10000
	v_add_u32_e32 v0, s25, v137
	s_add_u32 s39, s9, s29
	ds_read_b128 v[140:143], v0
	ds_read_b128 v[146:149], v0 offset:1024
	ds_read_b128 v[150:153], v0 offset:2048
	ds_read_b128 v[154:157], v0 offset:3072
	s_addc_u32 s51, s21, s30
	s_add_u32 s50, s39, 0xffffff80
	s_addc_u32 s51, s51, -1
	s_add_i32 s66, s25, s17
	s_add_i32 m0, s26, 0xc000
	s_add_i32 s39, s26, 0xe000
	s_add_i32 s64, 0, 0x14000
	s_add_i32 s67, s66, 0x2000
	s_cmp_eq_u32 s59, s24
	s_cselect_b32 s24, s42, s14
	s_cselect_b32 s25, s43, s15
	s_cselect_b32 s14, 0, s30
	s_cselect_b32 s15, 0, s29
	v_mov_b32_e32 v0, v132
	ds_read_b128 v[158:161], v139
	ds_read_b128 v[162:165], v139 offset:1024
	ds_read_b128 v[166:169], v139 offset:2048
	ds_read_b128 v[170:173], v139 offset:3072
	ds_read_b128 v[190:193], v139 offset:4096
	ds_read_b128 v[194:197], v139 offset:5120
	ds_read_b128 v[198:201], v139 offset:6144
	ds_read_b128 v[202:205], v139 offset:7168
	s_nop 0
	global_load_lds_dwordx4 v0, s[50:51]
	v_mov_b32_e32 v0, v134
	s_mov_b32 m0, s39
	s_nop 0
	global_load_lds_dwordx4 v0, s[50:51]
	s_waitcnt lgkmcnt(8)
	s_barrier
	s_waitcnt lgkmcnt(0)
	s_setprio 1
	s_waitcnt lgkmcnt(0)
	v_mfma_f32_16x16x32_bf16 v[128:131], v[140:143], v[158:161], v[128:131]
	v_mfma_f32_16x16x32_bf16 v[124:127], v[150:153], v[158:161], v[124:127]
	v_mfma_f32_16x16x32_bf16 v[112:115], v[140:143], v[166:169], v[112:115]
	v_mfma_f32_16x16x32_bf16 v[108:111], v[150:153], v[166:169], v[108:111]
	v_mfma_f32_16x16x32_bf16 v[96:99], v[140:143], v[190:193], v[96:99]
	v_mfma_f32_16x16x32_bf16 v[92:95], v[150:153], v[190:193], v[92:95]
	v_mfma_f32_16x16x32_bf16 v[80:83], v[140:143], v[198:201], v[80:83]
	v_mfma_f32_16x16x32_bf16 v[76:79], v[150:153], v[198:201], v[76:79]
	v_mfma_f32_16x16x32_bf16 v[128:131], v[146:149], v[162:165], v[128:131]
	v_mfma_f32_16x16x32_bf16 v[124:127], v[154:157], v[162:165], v[124:127]
	v_mfma_f32_16x16x32_bf16 v[112:115], v[146:149], v[170:173], v[112:115]
	v_mfma_f32_16x16x32_bf16 v[108:111], v[154:157], v[170:173], v[108:111]
	v_mfma_f32_16x16x32_bf16 v[96:99], v[146:149], v[194:197], v[96:99]
	v_mfma_f32_16x16x32_bf16 v[92:95], v[154:157], v[194:197], v[92:95]
	v_mfma_f32_16x16x32_bf16 v[80:83], v[146:149], v[202:205], v[80:83]
	v_mfma_f32_16x16x32_bf16 v[76:79], v[154:157], v[202:205], v[76:79]
	s_setprio 0
	s_barrier
	v_add_u32_e32 v0, s64, v137
	ds_read_b128 v[206:209], v0
	ds_read_b128 v[210:213], v0 offset:1024
	ds_read_b128 v[214:217], v0 offset:2048
	ds_read_b128 v[218:221], v0 offset:3072
	s_mov_b64 s[50:51], s[24:25]
	v_mov_b32_e32 v0, v133
	s_mov_b32 m0, s66
	s_nop 0
	global_load_lds_dwordx4 v0, s[50:51]
	v_mov_b32_e32 v0, v135
	s_mov_b32 m0, s67
	s_nop 0
	global_load_lds_dwordx4 v0, s[50:51]
	s_barrier
	s_waitcnt lgkmcnt(0)
	s_setprio 1
	s_waitcnt lgkmcnt(0)
	v_mfma_f32_16x16x32_bf16 v[120:123], v[206:209], v[158:161], v[120:123]
	v_mfma_f32_16x16x32_bf16 v[116:119], v[214:217], v[158:161], v[116:119]
	v_mfma_f32_16x16x32_bf16 v[104:107], v[206:209], v[166:169], v[104:107]
	v_mfma_f32_16x16x32_bf16 v[100:103], v[214:217], v[166:169], v[100:103]
	v_mfma_f32_16x16x32_bf16 v[88:91], v[206:209], v[190:193], v[88:91]
	v_mfma_f32_16x16x32_bf16 v[84:87], v[214:217], v[190:193], v[84:87]
	v_mfma_f32_16x16x32_bf16 v[72:75], v[206:209], v[198:201], v[72:75]
	v_mfma_f32_16x16x32_bf16 v[68:71], v[214:217], v[198:201], v[68:71]
	v_mfma_f32_16x16x32_bf16 v[120:123], v[210:213], v[162:165], v[120:123]
	v_mfma_f32_16x16x32_bf16 v[116:119], v[218:221], v[162:165], v[116:119]
	v_mfma_f32_16x16x32_bf16 v[104:107], v[210:213], v[170:173], v[104:107]
	v_mfma_f32_16x16x32_bf16 v[100:103], v[218:221], v[170:173], v[100:103]
	v_mfma_f32_16x16x32_bf16 v[88:91], v[210:213], v[194:197], v[88:91]
	v_mfma_f32_16x16x32_bf16 v[84:87], v[218:221], v[194:197], v[84:87]
	v_mfma_f32_16x16x32_bf16 v[72:75], v[210:213], v[202:205], v[72:75]
	v_mfma_f32_16x16x32_bf16 v[68:71], v[218:221], v[202:205], v[68:71]
	s_setprio 0
	s_cselect_b32 s69, s44, s48
	s_cselect_b32 s39, s45, s49
	s_add_u32 s50, s69, s15
	s_addc_u32 s51, s39, s14
	s_mov_b64 s[66:67], s[50:51]
	v_mov_b32_e32 v0, v132
	s_mov_b32 m0, s26
	s_barrier
	ds_read_b128 v[158:161], v139 offset:16384
	ds_read_b128 v[162:165], v139 offset:17408
	ds_read_b128 v[166:169], v139 offset:18432
	ds_read_b128 v[170:173], v139 offset:19456
	ds_read_b128 v[190:193], v139 offset:20480
	ds_read_b128 v[194:197], v139 offset:21504
	ds_read_b128 v[198:201], v139 offset:22528
	ds_read_b128 v[202:205], v139 offset:23552
	s_nop 0
	global_load_lds_dwordx4 v0, s[66:67]
	v_mov_b32_e32 v0, v134
	s_mov_b32 m0, s27
	s_nop 0
	global_load_lds_dwordx4 v0, s[66:67]
	s_barrier
	s_waitcnt lgkmcnt(0)
	s_setprio 1
	s_waitcnt lgkmcnt(0)
	v_mfma_f32_16x16x32_bf16 v[64:67], v[140:143], v[158:161], v[64:67]
	v_mfma_f32_16x16x32_bf16 v[60:63], v[150:153], v[158:161], v[60:63]
	v_mfma_f32_16x16x32_bf16 v[48:51], v[140:143], v[166:169], v[48:51]
	v_mfma_f32_16x16x32_bf16 v[44:47], v[150:153], v[166:169], v[44:47]
	v_mfma_f32_16x16x32_bf16 v[32:35], v[140:143], v[190:193], v[32:35]
	v_mfma_f32_16x16x32_bf16 v[28:31], v[150:153], v[190:193], v[28:31]
	v_mfma_f32_16x16x32_bf16 v[16:19], v[140:143], v[198:201], v[16:19]
	v_mfma_f32_16x16x32_bf16 v[12:15], v[150:153], v[198:201], v[12:15]
	v_mfma_f32_16x16x32_bf16 v[64:67], v[146:149], v[162:165], v[64:67]
	v_mfma_f32_16x16x32_bf16 v[60:63], v[154:157], v[162:165], v[60:63]
	v_mfma_f32_16x16x32_bf16 v[48:51], v[146:149], v[170:173], v[48:51]
	v_mfma_f32_16x16x32_bf16 v[44:47], v[154:157], v[170:173], v[44:47]
	v_mfma_f32_16x16x32_bf16 v[32:35], v[146:149], v[194:197], v[32:35]
	v_mfma_f32_16x16x32_bf16 v[28:31], v[154:157], v[194:197], v[28:31]
	v_mfma_f32_16x16x32_bf16 v[16:19], v[146:149], v[202:205], v[16:19]
	v_mfma_f32_16x16x32_bf16 v[12:15], v[154:157], v[202:205], v[12:15]
	s_setprio 0
	s_barrier
	s_add_u32 s66, s24, s4
	s_addc_u32 s67, s25, s5
	v_mov_b32_e32 v0, v133
	s_add_i32 s64, s64, s17
	s_mov_b32 m0, s64
	s_nop 0
	global_load_lds_dwordx4 v0, s[66:67]
	v_mov_b32_e32 v0, v135
	s_add_i32 m0, s64, 0x2000
	s_nop 0
	global_load_lds_dwordx4 v0, s[66:67]
	s_barrier
	s_setprio 1
	v_mfma_f32_16x16x32_bf16 v[56:59], v[206:209], v[158:161], v[56:59]
	v_mfma_f32_16x16x32_bf16 v[52:55], v[214:217], v[158:161], v[52:55]
	v_mfma_f32_16x16x32_bf16 v[40:43], v[206:209], v[166:169], v[40:43]
	v_mfma_f32_16x16x32_bf16 v[36:39], v[214:217], v[166:169], v[36:39]
	v_mfma_f32_16x16x32_bf16 v[24:27], v[206:209], v[190:193], v[24:27]
	v_mfma_f32_16x16x32_bf16 v[20:23], v[214:217], v[190:193], v[20:23]
	v_mfma_f32_16x16x32_bf16 v[8:11], v[206:209], v[198:201], v[8:11]
	v_mfma_f32_16x16x32_bf16 v[4:7], v[214:217], v[198:201], v[4:7]
	v_mfma_f32_16x16x32_bf16 v[56:59], v[210:213], v[162:165], v[56:59]
	v_mfma_f32_16x16x32_bf16 v[52:55], v[218:221], v[162:165], v[52:55]
	v_mfma_f32_16x16x32_bf16 v[40:43], v[210:213], v[170:173], v[40:43]
	v_mfma_f32_16x16x32_bf16 v[36:39], v[218:221], v[170:173], v[36:39]
	v_mfma_f32_16x16x32_bf16 v[24:27], v[210:213], v[194:197], v[24:27]
	v_mfma_f32_16x16x32_bf16 v[20:23], v[218:221], v[194:197], v[20:23]
	v_mfma_f32_16x16x32_bf16 v[8:11], v[210:213], v[202:205], v[8:11]
	v_mfma_f32_16x16x32_bf16 v[4:7], v[218:221], v[202:205], v[4:7]
	s_setprio 0
	s_add_i32 s64, 0, 0x18000
	v_add_u32_e32 v0, s64, v137
	s_waitcnt vmcnt(6)
	s_barrier
	ds_read_b128 v[140:143], v0
	ds_read_b128 v[146:149], v0 offset:1024
	ds_read_b128 v[150:153], v0 offset:2048
	ds_read_b128 v[154:157], v0 offset:3072
	s_add_u32 s66, s69, s0
	s_addc_u32 s39, s39, s1
	s_add_u32 s66, s66, s15
	s_addc_u32 s67, s39, s14
	v_mov_b32_e32 v0, v132
	s_mov_b32 m0, s52
	ds_read_b128 v[158:161], v139 offset:32768
	ds_read_b128 v[162:165], v139 offset:33792
	ds_read_b128 v[166:169], v139 offset:34816
	ds_read_b128 v[170:173], v139 offset:35840
	ds_read_b128 v[190:193], v139 offset:36864
	ds_read_b128 v[194:197], v139 offset:37888
	ds_read_b128 v[198:201], v139 offset:38912
	ds_read_b128 v[202:205], v139 offset:39936
	s_nop 0
	global_load_lds_dwordx4 v0, s[66:67]
	v_mov_b32_e32 v0, v134
	s_mov_b32 m0, s53
	s_nop 0
	global_load_lds_dwordx4 v0, s[66:67]
	s_waitcnt lgkmcnt(8)
	s_barrier
	s_waitcnt lgkmcnt(0)
	s_setprio 1
	s_waitcnt lgkmcnt(0)
	v_mfma_f32_16x16x32_bf16 v[128:131], v[140:143], v[158:161], v[128:131]
	v_mfma_f32_16x16x32_bf16 v[124:127], v[150:153], v[158:161], v[124:127]
	v_mfma_f32_16x16x32_bf16 v[112:115], v[140:143], v[166:169], v[112:115]
	v_mfma_f32_16x16x32_bf16 v[108:111], v[150:153], v[166:169], v[108:111]
	v_mfma_f32_16x16x32_bf16 v[96:99], v[140:143], v[190:193], v[96:99]
	v_mfma_f32_16x16x32_bf16 v[92:95], v[150:153], v[190:193], v[92:95]
	v_mfma_f32_16x16x32_bf16 v[80:83], v[140:143], v[198:201], v[80:83]
	v_mfma_f32_16x16x32_bf16 v[76:79], v[150:153], v[198:201], v[76:79]
	v_mfma_f32_16x16x32_bf16 v[128:131], v[146:149], v[162:165], v[128:131]
	v_mfma_f32_16x16x32_bf16 v[124:127], v[154:157], v[162:165], v[124:127]
	v_mfma_f32_16x16x32_bf16 v[112:115], v[146:149], v[170:173], v[112:115]
	v_mfma_f32_16x16x32_bf16 v[108:111], v[154:157], v[170:173], v[108:111]
	v_mfma_f32_16x16x32_bf16 v[96:99], v[146:149], v[194:197], v[96:99]
	v_mfma_f32_16x16x32_bf16 v[92:95], v[154:157], v[194:197], v[92:95]
	v_mfma_f32_16x16x32_bf16 v[80:83], v[146:149], v[202:205], v[80:83]
	v_mfma_f32_16x16x32_bf16 v[76:79], v[154:157], v[202:205], v[76:79]
	s_setprio 0
	s_barrier
	s_add_i32 s14, 0, 0x1c000
	s_add_u32 s24, s24, 0x80
	v_add_u32_e32 v0, s14, v137
	s_addc_u32 s25, s25, 0
	ds_read_b128 v[206:209], v0
	ds_read_b128 v[210:213], v0 offset:1024
	ds_read_b128 v[214:217], v0 offset:2048
	ds_read_b128 v[218:221], v0 offset:3072
	s_mov_b64 s[66:67], s[24:25]
	v_mov_b32_e32 v0, v133
	s_add_i32 s15, s64, s17
	s_mov_b32 m0, s15
	s_nop 0
	global_load_lds_dwordx4 v0, s[66:67]
	v_mov_b32_e32 v0, v135
	s_add_i32 m0, s15, 0x2000
	s_nop 0
	global_load_lds_dwordx4 v0, s[66:67]
	s_barrier
	s_waitcnt lgkmcnt(0)
	s_setprio 1
	s_waitcnt lgkmcnt(0)
	v_mfma_f32_16x16x32_bf16 v[120:123], v[206:209], v[158:161], v[120:123]
	v_mfma_f32_16x16x32_bf16 v[116:119], v[214:217], v[158:161], v[116:119]
	v_mfma_f32_16x16x32_bf16 v[104:107], v[206:209], v[166:169], v[104:107]
	v_mfma_f32_16x16x32_bf16 v[100:103], v[214:217], v[166:169], v[100:103]
	v_mfma_f32_16x16x32_bf16 v[88:91], v[206:209], v[190:193], v[88:91]
	v_mfma_f32_16x16x32_bf16 v[84:87], v[214:217], v[190:193], v[84:87]
	v_mfma_f32_16x16x32_bf16 v[72:75], v[206:209], v[198:201], v[72:75]
	v_mfma_f32_16x16x32_bf16 v[68:71], v[214:217], v[198:201], v[68:71]
	v_mfma_f32_16x16x32_bf16 v[120:123], v[210:213], v[162:165], v[120:123]
	v_mfma_f32_16x16x32_bf16 v[116:119], v[218:221], v[162:165], v[116:119]
	v_mfma_f32_16x16x32_bf16 v[104:107], v[210:213], v[170:173], v[104:107]
	v_mfma_f32_16x16x32_bf16 v[100:103], v[218:221], v[170:173], v[100:103]
	v_mfma_f32_16x16x32_bf16 v[88:91], v[210:213], v[194:197], v[88:91]
	v_mfma_f32_16x16x32_bf16 v[84:87], v[218:221], v[194:197], v[84:87]
	v_mfma_f32_16x16x32_bf16 v[72:75], v[210:213], v[202:205], v[72:75]
	v_mfma_f32_16x16x32_bf16 v[68:71], v[218:221], v[202:205], v[68:71]
	s_setprio 0
	s_add_u32 s50, s50, 0x80
	s_addc_u32 s51, s51, 0
	v_mov_b32_e32 v0, v132
	s_mov_b32 m0, s55
	s_barrier
	ds_read_b128 v[158:161], v139 offset:49152
	ds_read_b128 v[162:165], v139 offset:50176
	ds_read_b128 v[166:169], v139 offset:51200
	ds_read_b128 v[170:173], v139 offset:52224
	ds_read_b128 v[190:193], v139 offset:53248
	ds_read_b128 v[194:197], v139 offset:54272
	ds_read_b128 v[198:201], v139 offset:55296
	ds_read_b128 v[202:205], v139 offset:56320
	s_nop 0
	global_load_lds_dwordx4 v0, s[50:51]
	v_mov_b32_e32 v0, v134
	s_mov_b32 m0, s56
	s_nop 0
	global_load_lds_dwordx4 v0, s[50:51]
	s_barrier
	s_waitcnt lgkmcnt(0)
	s_setprio 1
	s_waitcnt lgkmcnt(0)
	v_mfma_f32_16x16x32_bf16 v[64:67], v[140:143], v[158:161], v[64:67]
	v_mfma_f32_16x16x32_bf16 v[60:63], v[150:153], v[158:161], v[60:63]
	v_mfma_f32_16x16x32_bf16 v[48:51], v[140:143], v[166:169], v[48:51]
	v_mfma_f32_16x16x32_bf16 v[44:47], v[150:153], v[166:169], v[44:47]
	v_mfma_f32_16x16x32_bf16 v[32:35], v[140:143], v[190:193], v[32:35]
	v_mfma_f32_16x16x32_bf16 v[28:31], v[150:153], v[190:193], v[28:31]
	v_mfma_f32_16x16x32_bf16 v[16:19], v[140:143], v[198:201], v[16:19]
	v_mfma_f32_16x16x32_bf16 v[12:15], v[150:153], v[198:201], v[12:15]
	v_mfma_f32_16x16x32_bf16 v[64:67], v[146:149], v[162:165], v[64:67]
	v_mfma_f32_16x16x32_bf16 v[60:63], v[154:157], v[162:165], v[60:63]
	v_mfma_f32_16x16x32_bf16 v[48:51], v[146:149], v[170:173], v[48:51]
	v_mfma_f32_16x16x32_bf16 v[44:47], v[154:157], v[170:173], v[44:47]
	v_mfma_f32_16x16x32_bf16 v[32:35], v[146:149], v[194:197], v[32:35]
	v_mfma_f32_16x16x32_bf16 v[28:31], v[154:157], v[194:197], v[28:31]
	v_mfma_f32_16x16x32_bf16 v[16:19], v[146:149], v[202:205], v[16:19]
	v_mfma_f32_16x16x32_bf16 v[12:15], v[154:157], v[202:205], v[12:15]
	s_setprio 0
	s_barrier
	s_add_u32 s24, s24, s4
	s_addc_u32 s25, s25, s5
	v_mov_b32_e32 v0, v133
	s_add_i32 s14, s14, s17
	s_mov_b32 m0, s14
	s_nop 0
	global_load_lds_dwordx4 v0, s[24:25]
	v_mov_b32_e32 v0, v135
	s_add_i32 m0, s14, 0x2000
	s_nop 0
	global_load_lds_dwordx4 v0, s[24:25]
	s_barrier
	s_setprio 1
	v_mfma_f32_16x16x32_bf16 v[56:59], v[206:209], v[158:161], v[56:59]
	v_mfma_f32_16x16x32_bf16 v[52:55], v[214:217], v[158:161], v[52:55]
	v_mfma_f32_16x16x32_bf16 v[40:43], v[206:209], v[166:169], v[40:43]
	v_mfma_f32_16x16x32_bf16 v[36:39], v[214:217], v[166:169], v[36:39]
	v_mfma_f32_16x16x32_bf16 v[24:27], v[206:209], v[190:193], v[24:27]
	v_mfma_f32_16x16x32_bf16 v[20:23], v[214:217], v[190:193], v[20:23]
	v_mfma_f32_16x16x32_bf16 v[8:11], v[206:209], v[198:201], v[8:11]
	v_mfma_f32_16x16x32_bf16 v[4:7], v[214:217], v[198:201], v[4:7]
	v_mfma_f32_16x16x32_bf16 v[56:59], v[210:213], v[162:165], v[56:59]
	v_mfma_f32_16x16x32_bf16 v[52:55], v[218:221], v[162:165], v[52:55]
	v_mfma_f32_16x16x32_bf16 v[40:43], v[210:213], v[170:173], v[40:43]
	v_mfma_f32_16x16x32_bf16 v[36:39], v[218:221], v[170:173], v[36:39]
	v_mfma_f32_16x16x32_bf16 v[24:27], v[210:213], v[194:197], v[24:27]
	v_mfma_f32_16x16x32_bf16 v[20:23], v[218:221], v[194:197], v[20:23]
	v_mfma_f32_16x16x32_bf16 v[8:11], v[210:213], v[202:205], v[8:11]
	v_mfma_f32_16x16x32_bf16 v[4:7], v[218:221], v[202:205], v[4:7]
	s_setprio 0
	s_add_u32 s29, s29, 0x100
	s_addc_u32 s30, s30, 0
	s_cmp_lt_i32 s31, s54
	s_mov_b32 s24, s31
	s_waitcnt vmcnt(6)
	s_barrier
	s_cbranch_scc1 .LBB0_1628
	s_mov_b32 s39, 0x8000
	s_and_b64 vcc, exec, s[40:41]
	s_cbranch_vccz .LBB0_1633
	s_branch .LBB0_1634
